# x f16 relocated to ws+96MiB so ws+0 only ever holds y (no region aliasing); c_proj_w pointer slot = first 8 bytes of y; sc1 write-through on cvt3 + q/k/v stores, y plain
# speedup vs baseline: 1.4681x; 1.4681x over previous
.LBB0_4:
	s_cmp_lg_u32 s3, 0
	s_cbranch_scc1 .LBB0_16
	s_load_dwordx2 s[4:5], s[0:1], 0x30
	s_load_dwordx2 s[6:7], s[0:1], 0x8
	s_waitcnt lgkmcnt(0)
	v_mov_b32_e32 v2, s4
	v_mov_b32_e32 v3, s5
	v_mov_b32_e32 v4, 0
	global_store_dwordx2 v4, v[2:3], s[6:7]
	s_branch .LBB0_16
.LBB0_5:
	s_load_dwordx4 s[4:7], s[0:1], 0x0
	s_mov_b32 s12, 0x6000000
	s_branch .LBB0_9

.LBB0_7:
	s_load_dwordx4 s[4:7], s[0:1], 0x18
	s_mov_b32 s12, 0
	s_sub_i32 s3, s8, s9

.LBB0_9:
	s_ashr_i32 s9, s8, 31
	s_lshl_b64 s[10:11], s[8:9], 14
	s_waitcnt lgkmcnt(0)
	s_add_u32 s6, s6, s12
	s_addc_u32 s7, s7, 0
	s_add_u32 s4, s4, s10
	s_addc_u32 s5, s5, s11
	v_lshlrev_b32_e32 v18, 4, v0
	v_mov_b32_e32 v19, 0
	v_lshl_add_u64 v[14:15], s[4:5], 0, v[18:19]
	s_movk_i32 s3, 0x2000
	v_add_co_u32_e32 v16, vcc, s3, v14
	s_movk_i32 s3, 0x3000
	s_nop 0
	v_addc_co_u32_e32 v17, vcc, 0, v15, vcc
	global_load_dwordx4 v[2:5], v18, s[4:5] nt
	v_add_co_u32_e32 v14, vcc, s3, v14
	global_load_dwordx4 v[6:9], v[16:17], off offset:-4096 nt
	global_load_dwordx4 v[10:13], v[16:17], off nt
	v_addc_co_u32_e32 v15, vcc, 0, v15, vcc
	global_load_dwordx4 v[14:17], v[14:15], off nt
	s_lshl_b64 s[4:5], s[8:9], 13
	s_add_u32 s4, s6, s4
	s_addc_u32 s5, s7, s5
	v_lshlrev_b32_e32 v18, 3, v0
	v_lshl_add_u64 v[20:21], s[4:5], 0, v[18:19]
	v_add_co_u32_e32 v20, vcc, 0x1000, v20
	s_waitcnt vmcnt(3)
	v_cvt_pk_f16_f32 v2, v2, v3
	v_cvt_pk_f16_f32 v3, v4, v5
	global_store_dwordx2 v18, v[2:3], s[4:5] sc1
	s_waitcnt vmcnt(3)
	v_cvt_pk_f16_f32 v2, v6, v7
	v_cvt_pk_f16_f32 v3, v8, v9
	v_addc_co_u32_e32 v21, vcc, 0, v21, vcc
	s_waitcnt vmcnt(2)
	v_cvt_pk_f16_f32 v4, v10, v11
	v_cvt_pk_f16_f32 v5, v12, v13
	s_waitcnt vmcnt(1)
	v_cvt_pk_f16_f32 v6, v14, v15
	v_cvt_pk_f16_f32 v7, v16, v17
	global_store_dwordx2 v18, v[2:3], s[4:5] offset:2048 sc1
	global_store_dwordx2 v[20:21], v[4:5], off sc1
	global_store_dwordx2 v[20:21], v[6:7], off offset:2048 sc1
	s_mov_b64 s[4:5], 0

	.amdhsa_kernel _Z8cvt3_f16PKfPDF16_iS0_S1_iS0_S1_iPfS2_
		.amdhsa_group_segment_fixed_size 0
		.amdhsa_private_segment_fixed_size 0
		.amdhsa_kernarg_size 88
		.amdhsa_user_sgpr_count 2
		.amdhsa_user_sgpr_dispatch_ptr 0
		.amdhsa_user_sgpr_queue_ptr 0
		.amdhsa_user_sgpr_kernarg_segment_ptr 1
		.amdhsa_user_sgpr_dispatch_id 0
		.amdhsa_user_sgpr_kernarg_preload_length 0
		.amdhsa_user_sgpr_kernarg_preload_offset 0
		.amdhsa_user_sgpr_private_segment_size 0
		.amdhsa_uses_dynamic_stack 0
		.amdhsa_enable_private_segment 0
		.amdhsa_system_sgpr_workgroup_id_x 1
		.amdhsa_system_sgpr_workgroup_id_y 0
		.amdhsa_system_sgpr_workgroup_id_z 0
		.amdhsa_system_sgpr_workgroup_info 0
		.amdhsa_system_vgpr_workitem_id 0
		.amdhsa_next_free_vgpr 24
		.amdhsa_next_free_sgpr 16
		.amdhsa_accum_offset 24
		.amdhsa_reserve_vcc 1
		.amdhsa_float_round_mode_32 0
		.amdhsa_float_round_mode_16_64 0
		.amdhsa_float_denorm_mode_32 3
		.amdhsa_float_denorm_mode_16_64 3
		.amdhsa_dx10_clamp 1
		.amdhsa_ieee_mode 1
		.amdhsa_fp16_overflow 0
		.amdhsa_tg_split 0
		.amdhsa_exception_fp_ieee_invalid_op 0
		.amdhsa_exception_fp_denorm_src 0
		.amdhsa_exception_fp_ieee_div_zero 0
		.amdhsa_exception_fp_ieee_overflow 0
		.amdhsa_exception_fp_ieee_underflow 0
		.amdhsa_exception_fp_ieee_inexact 0
		.amdhsa_exception_int_div_zero 0
	.end_amdhsa_kernel

_Z8gemm_qkvPKDF16_S0_7EpiArgs:
	s_load_dwordx4 s[4:7], s[0:1], 0x0
	s_lshr_b32 s3, s2, 8
	s_and_b32 s10, s2, 31
	s_lshr_b32 s11, s2, 1
	s_and_b32 s11, s11, 0x60
	s_or_b32 s10, s10, s11
	s_and_b32 s11, s2, 0x7f
	s_cmp_eq_u32 s3, 0
	s_cselect_b32 s10, s10, s11
	s_cselect_b32 s11, 5, 7
	s_lshr_b32 s11, s2, s11
	s_and_b32 s11, s11, 1
	s_and_b32 s2, s10, 31
	s_lshl_b32 s3, s3, 5
	s_or_b32 s2, s2, s3
	s_and_b32 s10, s10, 0x60
	s_lshl_b32 s10, s10, 1
	s_or_b32 s2, s2, s10
	s_lshl_b32 s11, s11, 8
	s_or_b32 s2, s2, s11
	s_waitcnt lgkmcnt(0)
	s_add_u32 s4, s4, 0x6000000
	s_addc_u32 s5, s5, 0
	s_cmpk_gt_u32 s2, 0xff
	s_waitcnt lgkmcnt(0)
	s_mov_b64 s[8:9], s[6:7]
	s_mov_b64 s[6:7], -1
	s_cbranch_scc1 .LBB2_3
	s_and_b64 vcc, exec, s[6:7]
	s_cbranch_vccnz .LBB2_16

.LBB3_2:
	s_and_b32 s96, s8, 3
	s_lshl_b32 s9, s4, 14
	s_cmp_lg_u32 0, -1
	s_cselect_b32 s10, 0, 0
	s_lshl_b64 s[0:1], s[0:1], 1
	s_add_u32 s72, s64, s0
	s_addc_u32 s11, s65, s1
	s_add_i32 s8, s9, 0
	s_bfe_u32 s33, s2, 0x40003
	s_add_i32 s12, s8, 0x10000
	s_add_u32 s64, s60, s0
	s_addc_u32 s65, s61, s1
	s_load_dwordx2 s[62:63], s[66:67], 0x0
	s_xor_b32 s99, s33, 31
	v_and_b32_e32 v207, 31, v0
	s_lshl_b32 s8, s99, 7
	v_lshlrev_b32_e32 v4, 4, v0
	v_bfe_u32 v160, v0, 5, 1
	s_lshl_b32 s79, s96, 5
	v_or_b32_e32 v11, s8, v207
	v_lshlrev_b32_e32 v184, 4, v160
	v_mov_b32_e32 v185, 0
	v_lshlrev_b32_e32 v5, 8, v207
	v_and_b32_e32 v6, 0x70, v4
	v_or_b32_e32 v161, s79, v11
	v_lshl_add_u64 v[2:3], s[64:65], 0, v[184:185]
	v_bitop3_b32 v7, v184, v5, v6 bitop3:0xde
	v_or_b32_e32 v8, 32, v184
	v_or_b32_e32 v9, 64, v184
	v_or_b32_e32 v10, 0x60, v184
	v_lshlrev_b32_e32 v184, 8, v161
	v_lshl_add_u64 v[2:3], v[2:3], 0, v[184:185]
	global_load_dwordx4 v[156:159], v[2:3], off
	global_load_dwordx4 v[152:155], v[2:3], off offset:32
	global_load_dwordx4 v[148:151], v[2:3], off offset:64
	global_load_dwordx4 v[144:147], v[2:3], off offset:96
	global_load_dwordx4 v[140:143], v[2:3], off offset:128
	global_load_dwordx4 v[136:139], v[2:3], off offset:160
	global_load_dwordx4 v[132:135], v[2:3], off offset:192
	global_load_dwordx4 v[128:131], v[2:3], off offset:224
	v_and_b32_e32 v2, 63, v0
	v_lshlrev_b32_e32 v2, 3, v2
	v_and_b32_e32 v4, 0xc0, v4
	v_lshlrev_b32_e32 v11, 1, v0
	v_and_b32_e32 v3, 24, v2
	v_and_b32_e32 v11, 32, v11
	v_add_u32_e32 v4, s10, v4
	v_add3_u32 v3, v4, v11, v3
	v_and_b32_e32 v4, 16, v1
	v_lshlrev_b32_e32 v1, 3, v1
	v_lshrrev_b32_e32 v11, 5, v0
	v_and_b32_e32 v1, 8, v1
	v_bfe_u32 v12, v0, 2, 2
	v_and_or_b32 v4, v11, 4, v4
	v_or3_b32 v1, v4, v12, v1
	v_and_b32_e32 v4, 0x60, v0
	v_lshlrev_b32_e32 v0, 3, v0
	v_and_or_b32 v0, v0, 24, v4
	v_lshlrev_b32_e32 v0, 1, v0
	v_lshl_or_b32 v186, v1, 8, v0
	v_bitop3_b32 v0, v8, v5, v6 bitop3:0xde
	v_add_u32_e32 v189, s12, v0
	v_bitop3_b32 v0, v9, v5, v6 bitop3:0xde
	s_waitcnt vmcnt(0) lgkmcnt(0)
	s_barrier
	s_lshl_b32 s101, s2, 16
	s_add_u32 s62, s62, s101
	s_addc_u32 s63, s63, 0
	s_lshl_b32 s101, s2, 15
	s_sub_u32 s60, s60, 0x800000
	s_subb_u32 s61, s61, 0
	s_add_u32 s60, s60, s101
	s_addc_u32 s61, s61, 0
	s_mov_b32 s100, 0
	v_and_b32_e32 v2, 0x100, v2
	v_add_u32_e32 v188, s12, v0
	v_bitop3_b32 v0, v10, v5, v6 bitop3:0xde
	v_add3_u32 v184, v3, v2, s9
	s_and_b32 s73, s11, 0xffff
	s_mov_b32 s74, s70
	s_mov_b32 s75, s71
	v_add_u32_e32 v190, s12, v7
	v_add_u32_e32 v187, s12, v0
	s_add_i32 s91, s3, 0x18000
	s_add_i32 s92, s3, 0x1a000
	s_add_i32 s93, s3, 0x1c000
	s_mov_b32 s0, 0x1e000
	s_add_i32 s94, s3, 0x1e000
	s_add_i32 s82, s3, 0x2000
	s_add_i32 s81, s3, 0x4000
	s_add_i32 s80, s3, 0x6000
	s_add_i32 s90, s3, 0x8000
	s_add_i32 s89, s3, 0xa000
	s_add_i32 s88, s3, 0xc000
	s_add_i32 s87, s3, 0xe000
	s_mov_b32 s1, 0x8000
	s_mov_b32 s9, 0xa000
	s_mov_b32 s10, 0xc000
	s_mov_b32 s11, 0xe000
	ds_read_b128 v[16:19], v190
	ds_read_b128 v[20:23], v190 offset:8192
	s_mov_b32 m0, s91
	s_waitcnt vmcnt(7) lgkmcnt(1)
	v_mfma_f32_32x32x16_f16 v[0:15], v[16:19], v[156:159], -0.5
	buffer_load_dwordx4 v191, s[68:71], s1 offen lds
	ds_read_b128 v[24:27], v189
	ds_read_b128 v[16:19], v189 offset:8192
	s_mov_b32 m0, s92
	s_waitcnt lgkmcnt(2)
	v_mfma_f32_32x32x16_f16 v[96:111], v[20:23], v[156:159], -0.5
	s_waitcnt vmcnt(7) lgkmcnt(1)
	v_mfma_f32_32x32x16_f16 v[0:15], v[24:27], v[152:155], v[0:15]
	buffer_load_dwordx4 v191, s[68:71], s9 offen lds
	s_mov_b32 m0, s93
	s_waitcnt lgkmcnt(0)
	v_mfma_f32_32x32x16_f16 v[96:111], v[16:19], v[152:155], v[96:111]
	ds_read_b128 v[16:19], v188
	s_waitcnt vmcnt(7) lgkmcnt(0)
	v_mfma_f32_32x32x16_f16 v[0:15], v[16:19], v[148:151], v[0:15]
	ds_read_b128 v[16:19], v188 offset:8192
	buffer_load_dwordx4 v191, s[68:71], s10 offen lds
	s_mov_b32 m0, s94
	s_waitcnt lgkmcnt(0)
	v_mfma_f32_32x32x16_f16 v[96:111], v[16:19], v[148:151], v[96:111]
	ds_read_b128 v[16:19], v187
	s_waitcnt vmcnt(7) lgkmcnt(0)
	v_mfma_f32_32x32x16_f16 v[0:15], v[16:19], v[144:147], v[0:15]
	ds_read_b128 v[16:19], v187 offset:8192
	buffer_load_dwordx4 v191, s[68:71], s11 offen lds
	s_mov_b32 m0, s3
	s_waitcnt lgkmcnt(0)
	v_mfma_f32_32x32x16_f16 v[96:111], v[16:19], v[144:147], v[96:111]
	ds_read_b128 v[16:19], v190 offset:128
	s_waitcnt vmcnt(7) lgkmcnt(0)
	v_mfma_f32_32x32x16_f16 v[0:15], v[16:19], v[140:143], v[0:15]
	ds_read_b128 v[16:19], v190 offset:8320
	buffer_load_dwordx4 v186, s[72:75], 0 offen lds
	s_mov_b32 m0, s82
	s_waitcnt lgkmcnt(0)
	v_mfma_f32_32x32x16_f16 v[96:111], v[16:19], v[140:143], v[96:111]
	ds_read_b128 v[16:19], v189 offset:128
	s_waitcnt vmcnt(7) lgkmcnt(0)
	v_mfma_f32_32x32x16_f16 v[0:15], v[16:19], v[136:139], v[0:15]
	ds_read_b128 v[16:19], v189 offset:8320
	buffer_load_dwordx4 v186, s[72:75], s7 offen lds
	s_mov_b32 m0, s81
	s_waitcnt lgkmcnt(0)
	v_mfma_f32_32x32x16_f16 v[96:111], v[16:19], v[136:139], v[96:111]
	ds_read_b128 v[16:19], v188 offset:128
	s_waitcnt vmcnt(7) lgkmcnt(0)
	v_mfma_f32_32x32x16_f16 v[0:15], v[16:19], v[132:135], v[0:15]
	ds_read_b128 v[16:19], v188 offset:8320
	buffer_load_dwordx4 v186, s[72:75], s6 offen lds
	s_mov_b32 m0, s80
	s_waitcnt lgkmcnt(0)
	v_mfma_f32_32x32x16_f16 v[96:111], v[16:19], v[132:135], v[96:111]
	ds_read_b128 v[16:19], v187 offset:128
	ds_read_b128 v[20:23], v187 offset:8320
	buffer_load_dwordx4 v186, s[72:75], s5 offen lds
	s_waitcnt vmcnt(0) lgkmcnt(0)
	s_barrier
	s_waitcnt vmcnt(8) lgkmcnt(0)
	v_mfma_f32_32x32x16_f16 v[96:111], v[20:23], v[128:131], v[96:111]
	v_mfma_f32_32x32x16_f16 v[0:15], v[16:19], v[128:131], v[0:15]
	s_nop 11
	v_exp_f32_e32 v210, v0
	v_exp_f32_e32 v211, v1
	v_exp_f32_e32 v212, v2
	v_exp_f32_e32 v213, v3
	v_exp_f32_e32 v214, v4
	v_exp_f32_e32 v215, v5
	v_exp_f32_e32 v216, v6
	v_exp_f32_e32 v217, v7
	v_exp_f32_e32 v218, v8
	v_exp_f32_e32 v219, v9
	v_exp_f32_e32 v220, v10
	v_exp_f32_e32 v221, v11
	v_exp_f32_e32 v222, v12
	v_exp_f32_e32 v223, v13
	v_exp_f32_e32 v224, v14
	v_exp_f32_e32 v225, v15
	v_mov_b32_e32 v16, v185
	v_mov_b32_e32 v17, v185
	v_mov_b32_e32 v18, v185
	v_mov_b32_e32 v19, v185
	v_mov_b32_e32 v20, v185
	v_mov_b32_e32 v21, v185
	v_mov_b32_e32 v22, v185
	v_mov_b32_e32 v23, v185
	v_mov_b32_e32 v24, v185
	v_mov_b32_e32 v25, v185
	v_mov_b32_e32 v26, v185
	v_mov_b32_e32 v27, v185
	v_mov_b32_e32 v28, v185
	v_mov_b32_e32 v29, v185
	v_mov_b32_e32 v30, v185
	v_mov_b32_e32 v31, v185
	v_mov_b32_e32 v32, v185
	v_mov_b32_e32 v33, v185
	v_mov_b32_e32 v34, v185
	v_mov_b32_e32 v35, v185
	v_mov_b32_e32 v36, v185
	v_mov_b32_e32 v37, v185
	v_mov_b32_e32 v38, v185
	v_mov_b32_e32 v39, v185
	v_mov_b32_e32 v40, v185
	v_mov_b32_e32 v41, v185
	v_mov_b32_e32 v42, v185
	v_mov_b32_e32 v43, v185
	v_mov_b32_e32 v44, v185
	v_mov_b32_e32 v45, v185
	v_mov_b32_e32 v46, v185
	v_mov_b32_e32 v47, v185
	v_mov_b32_e32 v48, v185
	v_mov_b32_e32 v49, v185
	v_mov_b32_e32 v50, v185
	v_mov_b32_e32 v51, v185
	v_mov_b32_e32 v52, v185
	v_mov_b32_e32 v53, v185
	v_mov_b32_e32 v54, v185
	v_mov_b32_e32 v55, v185
	v_mov_b32_e32 v56, v185
	v_mov_b32_e32 v57, v185
	v_mov_b32_e32 v58, v185
	v_mov_b32_e32 v59, v185
	v_mov_b32_e32 v60, v185
	v_mov_b32_e32 v61, v185
	v_mov_b32_e32 v62, v185
	v_mov_b32_e32 v63, v185
	v_mov_b32_e32 v64, v185
	v_mov_b32_e32 v65, v185
	v_mov_b32_e32 v66, v185
	v_mov_b32_e32 v67, v185
	v_mov_b32_e32 v68, v185
	v_mov_b32_e32 v69, v185
	v_mov_b32_e32 v70, v185
	v_mov_b32_e32 v71, v185
	v_mov_b32_e32 v72, v185
	v_mov_b32_e32 v73, v185
	v_mov_b32_e32 v74, v185
	v_mov_b32_e32 v75, v185
	v_mov_b32_e32 v76, v185
	v_mov_b32_e32 v77, v185
	v_mov_b32_e32 v78, v185
	v_mov_b32_e32 v79, v185
